# v59 + one static s_setprio 1 for waves 4-7 through the attention phase (reset before conversion and before P3)
# speedup vs baseline: 1.0045x; 1.0030x over previous
.LBB0_266:
	s_and_b64 vcc, exec, s[0:1]
	s_mov_b64 s[0:1], -1
	s_cbranch_vccnz .LBB0_276
	s_setprio 0
	s_mov_b32 s27, 1
	s_mov_b32 s32, s74
	s_mov_b32 s33, s75
	s_mov_b32 s34, s78
	s_mov_b32 s35, s79
	s_mov_b32 s36, s82
	s_mov_b32 s37, s83
	s_mov_b32 s42, s90
	s_mov_b32 s43, s91
	s_mov_b32 s95, 0x900
	s_branch .Lcva_entry

.LBB0_276:
	s_and_b64 vcc, exec, s[0:1]
	s_cbranch_vccz .LBB0_265
	v_readlane_b32 s98, v255, 4
	s_nop 3
	s_cmp_ge_u32 s98, 0x100
	s_cbranch_scc0 .Lp2_prio_done
	s_setprio 1
.Lp2_prio_done:
	v_readlane_b32 s0, v255, 4
	v_mbcnt_lo_u32_b32 v1, -1, 0
	v_mbcnt_hi_u32_b32 v1, -1, v1
	s_nop 1
	v_add_u32_e32 v168, s0, v1
	s_nop 0
	v_cmp_eq_u32_e64 s[0:1], 0, v168
	s_barrier
	s_and_saveexec_b64 s[4:5], s[0:1]
	s_cbranch_execz .LBB0_281
	s_mov_b64 s[8:9], exec
	v_mbcnt_lo_u32_b32 v1, s8, 0
	v_mbcnt_hi_u32_b32 v1, s9, v1
	v_cmp_eq_u32_e32 vcc, 0, v1
	s_and_saveexec_b64 s[6:7], vcc
	s_cbranch_execz .LBB0_280
	s_bcnt1_i32_b64 s8, s[8:9]
	v_mov_b32_e32 v2, s8
	global_atomic_add v2, v0, v2, s[90:91] offset:1280 sc0
	s_waitcnt vmcnt(0)
	v_writelane_b32 v255, 1, 60
	s_mov_b64 s[100:101], exec
	s_mov_b32 exec_lo, 0
	s_mov_b32 exec_hi, 0x10000000
	global_atomic_add v255, v0, v255, s[90:91] offset:1280 sc0
	s_mov_b64 exec, s[100:101]

.LBB0_411:
	s_setprio 0
	s_cmp_gt_i32 s14, 3
	s_cselect_b64 s[0:1], -1, 0
	s_cmp_lt_i32 s15, 4
	s_cselect_b64 s[2:3], -1, 0
	s_or_b64 s[0:1], s[0:1], s[2:3]
	s_and_b64 vcc, exec, s[0:1]
	s_cbranch_vccnz .LBB0_480
	v_readlane_b32 s0, v255, 4
	s_waitcnt vmcnt(11)
	v_mbcnt_lo_u32_b32 v0, -1, 0
	v_mbcnt_hi_u32_b32 v0, -1, v0
	s_waitcnt vmcnt(8)
	v_add_u32_e32 v32, s0, v0
	s_lshl_b32 s0, s92, 3
	s_add_i32 s4, s0, s94
	s_cmpk_gt_i32 s4, 0x1fff
	s_cbranch_scc1 .LBB0_427
	v_and_b32_e32 v36, 63, v32
	v_readlane_b32 s8, v255, 9
	v_lshlrev_b32_e32 v33, 5, v36
	v_readlane_b32 s14, v255, 15
	v_readlane_b32 s15, v255, 16
	v_readlane_b32 s16, v255, 17
	v_readlane_b32 s17, v255, 18
	s_nop 2
	global_load_dwordx4 v[0:3], v33, s[14:15]
	s_nop 0
	global_load_dwordx4 v[4:7], v33, s[16:17]
	global_load_dwordx4 v[8:11], v33, s[14:15] offset:16
	global_load_dwordx4 v[12:15], v33, s[16:17] offset:16
	global_load_dwordx4 v[16:19], v33, s[14:15] offset:2048
	global_load_dwordx4 v[20:23], v33, s[16:17] offset:2048
	global_load_dwordx4 v[24:27], v33, s[14:15] offset:2064
	global_load_dwordx4 v[28:31], v33, s[16:17] offset:2064
	v_lshrrev_b32_e32 v32, 1, v32
	v_and_b32_e32 v32, 28, v32
	v_mov_b32_e32 v33, 0
	v_lshl_add_u64 v[34:35], s[90:91], 0, v[32:33]
	s_mov_b64 s[0:1], 0x400000
	v_lshl_add_u64 v[160:161], v[34:35], 0, s[0:1]
	v_mov_b32_e32 v35, v33
	v_mbcnt_lo_u32_b32 v33, -1, 0
	v_lshlrev_b32_e32 v34, 4, v36
	v_mbcnt_hi_u32_b32 v33, -1, v33
	v_lshl_add_u64 v[36:37], s[90:91], 0, v[34:35]
	v_and_b32_e32 v35, 64, v33
	v_add_u32_e32 v35, 64, v35
	v_xor_b32_e32 v38, 1, v33
	v_cmp_lt_i32_e32 vcc, v38, v35
	s_mov_b64 s[0:1], 0x8800000
	v_lshl_add_u64 v[162:163], v[36:37], 0, s[0:1]
	v_cndmask_b32_e32 v38, v33, v38, vcc
	v_lshlrev_b32_e32 v175, 2, v38
	v_xor_b32_e32 v38, 2, v33
	v_cmp_lt_i32_e32 vcc, v38, v35
	s_mov_b64 s[0:1], 0xb800000
	v_lshl_add_u64 v[164:165], v[36:37], 0, s[0:1]
	v_cndmask_b32_e32 v38, v33, v38, vcc
	v_lshlrev_b32_e32 v176, 2, v38
	v_xor_b32_e32 v38, 4, v33
	v_cmp_lt_i32_e32 vcc, v38, v35
	s_mov_b64 s[0:1], 0xc800000
	s_ashr_i32 s5, s4, 31
	v_cndmask_b32_e32 v38, v33, v38, vcc
	v_lshlrev_b32_e32 v177, 2, v38
	v_xor_b32_e32 v38, 8, v33
	v_cmp_lt_i32_e32 vcc, v38, v35
	v_readlane_b32 s9, v255, 10
	s_mov_b64 s[6:7], s[14:15]
	v_cndmask_b32_e32 v38, v33, v38, vcc
	v_lshlrev_b32_e32 v178, 2, v38
	v_xor_b32_e32 v38, 16, v33
	v_cmp_lt_i32_e32 vcc, v38, v35
	v_lshl_add_u64 v[166:167], v[36:37], 0, s[0:1]
	s_lshl_b64 s[0:1], s[4:5], 12
	v_cndmask_b32_e32 v38, v33, v38, vcc
	v_lshlrev_b32_e32 v179, 2, v38
	v_xor_b32_e32 v38, 32, v33
	s_mov_b64 s[8:9], s[16:17]
	s_lshl_b32 s6, s70, 5
	v_cmp_lt_i32_e32 vcc, v38, v35
	v_or_b32_e32 v168, s0, v34
	v_mov_b32_e32 v169, s1
	s_lshl_b64 s[0:1], s[4:5], 11
	v_readlane_b32 s10, v255, 11
	v_readlane_b32 s11, v255, 12
	v_readlane_b32 s12, v255, 13
	v_readlane_b32 s13, v255, 14
	v_cndmask_b32_e32 v33, v33, v38, vcc
	s_ashr_i32 s7, s6, 31
	v_or_b32_e32 v170, s0, v34
	v_mov_b32_e32 v171, s1
	s_lshl_b64 s[0:1], s[4:5], 6
	s_lshl_b32 s2, s70, 3
	v_lshlrev_b32_e32 v180, 2, v33
	s_lshl_b32 s3, s70, 4
	s_mul_i32 s15, s70, 24
	s_lshl_b64 s[8:9], s[6:7], 12
	s_lshl_b64 s[10:11], s[6:7], 11
	v_or_b32_e32 v172, s0, v32
	v_mov_b32_e32 v173, s1
	s_lshl_b64 s[12:13], s[6:7], 6
	s_mov_b32 s5, 0x400000
	s_mov_b32 s7, 0x8800000
	s_mov_b32 s28, 0x480000
	s_mov_b32 s29, 0x9800000
	s_mov_b32 s30, 0x500000
	s_mov_b32 s14, 0x3a800000
	s_mov_b32 s31, 0x800000
	s_mov_b32 s33, 0xc800000
	v_mov_b32_e32 v174, 0x3727c5ac
	v_readlane_b32 s18, v255, 19
	v_readlane_b32 s19, v255, 20
	v_readlane_b32 s20, v255, 21
	v_readlane_b32 s21, v255, 22
	v_readlane_b32 s22, v255, 23
	v_readlane_b32 s23, v255, 24
	s_branch .LBB0_415
